# v055 + P0 row loop: next input row requested one trip ahead (was: load a row, wait for it, convert, store)
# baseline (speedup 1.0000x reference)
; __global__ void __launch_bounds__(NWAVES * 64, 2) mk_fwd(Args args) {
;     ...
;         const float* x = args.in[0];
;         for (int t = gw; t < T; t += NGW) {
;             float o[16];
; #pragma unroll
;             for (int hf = 0; hf < 2; ++hf) { const f32x4 a = *(const f32x4*)(x + (size_t)t * D + 512 * hf + 8 * lane), b = *(const f32x4*)(x + (size_t)t * D + 512 * hf + 8 * lane + 4);
.LBB0_29:
	v_readlane_b32 s0, v253, 19
	s_cmp_lt_i32 s0, 0x8000
	s_cselect_b64 s[2:3], -1, 0
	v_writelane_b32 v254, s2, 38
	s_cmpk_gt_i32 s0, 0x7fff
	v_readlane_b32 s1, v253, 20
	v_writelane_b32 v254, s3, 39
	s_cbranch_scc1 .LBB0_34
	v_readlane_b32 s2, v253, 19
	v_readlane_b32 s3, v253, 20
	s_mov_b32 s34, s2
	s_ashr_i32 s35, s2, 31
	s_lshl_b64 s[2:3], s[34:35], 2
	v_lshlrev_b32_e32 v4, 3, v0
	s_add_u32 s12, s2, 0x12180000
	v_ashrrev_i32_e32 v5, 31, v4
	s_addc_u32 s13, s3, 0
	s_lshl_b64 s[2:3], s[34:35], 11
	v_cmp_eq_u32_e64 s[0:1], 0, v0
	s_ashr_i32 s83, s82, 31
	v_lshl_add_u64 v[0:1], v[4:5], 1, s[2:3]
	s_lshl_b64 s[2:3], s[34:35], 10
	s_lshl_b64 s[4:5], s[82:83], 2
	s_lshl_b64 s[6:7], s[82:83], 11
	v_lshl_add_u64 v[2:3], s[2:3], 0, v[4:5]
	s_lshl_b64 s[8:9], s[82:83], 10
	s_lshl_b64 s[2:3], s[34:35], 12
	v_readlane_b32 s16, v252, 10
	v_readlane_b32 s17, v252, 11
	s_add_u32 s2, s16, s2
	s_addc_u32 s3, s17, s3
	v_lshl_add_u64 v[4:5], v[4:5], 2, s[2:3]
	s_mov_b32 s2, s34
	v_readlane_b32 s18, v252, 12
	v_writelane_b32 v253, s2, 19
	s_lshl_b64 s[10:11], s[82:83], 12
	s_mov_b32 s14, 0x32000000
	s_mov_b32 s15, 0xc0c0400
	s_mov_b32 s16, 0x5040100
	s_mov_b32 s17, 0x12200000
	v_mov_b32_e32 v6, 0
	v_writelane_b32 v253, s3, 20
	s_mov_b32 s18, s34
	v_readlane_b32 s19, v252, 13
	v_readlane_b32 s20, v252, 14
	v_readlane_b32 s21, v252, 15
	v_readlane_b32 s22, v252, 16
	v_readlane_b32 s23, v252, 17
	v_readlane_b32 s24, v252, 18
	v_readlane_b32 s25, v252, 19
	v_readlane_b32 s26, v252, 20
	v_readlane_b32 s27, v252, 21
	v_readlane_b32 s28, v252, 22
	v_readlane_b32 s29, v252, 23
	v_readlane_b32 s30, v252, 24
	v_readlane_b32 s31, v252, 25
	global_load_dwordx4 v[40:43], v[4:5], off
	global_load_dwordx4 v[44:47], v[4:5], off offset:16
	global_load_dwordx4 v[48:51], v[4:5], off offset:2048
	global_load_dwordx4 v[52:55], v[4:5], off offset:2064
	s_branch .LBB0_32

; __device__ __forceinline__ u32x4 pack8(const float (&f)[8]) { u32x4 o; o.x = cvt_pk_bf16(f[0], f[1]); o.y = cvt_pk_bf16(f[2], f[3]); o.z = cvt_pk_bf16(f[4], f[5]); o.w = cvt_pk_bf16(f[6], f[7]); return o; }
; __device__ __forceinline__ float wave_max(float v) { v = fmaxf(v, dpp_f<0xB1>(v)); v = fmaxf(v, dpp_f<0x4E>(v)); v = fmaxf(v, dpp_f<0x141>(v)); v = fmaxf(v, dpp_f<0x140>(v)); v = fmaxf(v, xor_sw<16>(v)); return max_x32(v); }
; __device__ __forceinline__ float q8_row16(const float (&o)[16], unsigned char* qrow, int lane) {
;     float am = 0.f;
; #pragma unroll
;     for (int i = 0; i < 16; ++i) am = fmaxf(am, fabsf(o[i]));
;     am = wave_max(am);
;     const float qs = am > 0.f ? am * (1.0f / 127.0f) : 1.0f, qinv = 1.0f / qs;
; #pragma unroll
;     for (int hf = 0; hf < 2; ++hf) { u32x2 q; q.x = q8x4(o[8 * hf], o[8 * hf + 1], o[8 * hf + 2], o[8 * hf + 3], qinv); q.y = q8x4(o[8 * hf + 4], o[8 * hf + 5], o[8 * hf + 6], o[8 * hf + 7], qinv);
;         *(u32x2*)(qrow + 512 * hf + 8 * lane) = q; }
;     return qs;
; }
; __device__ __forceinline__ void store_bf16_row16(const float (&o)[16], bf16_t* row, int lane) {
; #pragma unroll
;     for (int hf = 0; hf < 2; ++hf) { const float (&oh)[8] = *(const float (*)[8])(o + 8 * hf); *(u32x4*)(row + 512 * hf + 8 * lane) = pack8(oh); }
; __global__ void __launch_bounds__(NWAVES * 64, 2) mk_fwd(Args args) {
;     ...
;         for (int t = gw; t < T; t += NGW) {
;             float o[16];
; #pragma unroll
;             for (int hf = 0; hf < 2; ++hf) { const f32x4 a = *(const f32x4*)(x + (size_t)t * D + 512 * hf + 8 * lane), b = *(const f32x4*)(x + (size_t)t * D + 512 * hf + 8 * lane + 4);
; #pragma unroll
;                 for (int i = 0; i < 4; ++i) { o[8 * hf + i] = a[i]; o[8 * hf + 4 + i] = b[i]; } }
;             store_bf16_row16(o, XB + (size_t)t * D, lane);
;             const float qs = q8_row16(o, ws + WS_XQ + (size_t)t * D, lane);
;             if (lane == 0) ((float*)(ws + WS_SX))[t] = qs;
;         }
.LBB0_32:
	s_waitcnt vmcnt(0)
	v_mov_b64_e32 v[8:9], v[40:41]
	v_mov_b64_e32 v[10:11], v[42:43]
	v_mov_b64_e32 v[12:13], v[44:45]
	v_mov_b64_e32 v[14:15], v[46:47]
	v_mov_b64_e32 v[16:17], v[48:49]
	v_mov_b64_e32 v[18:19], v[50:51]
	v_mov_b64_e32 v[20:21], v[52:53]
	v_mov_b64_e32 v[22:23], v[54:55]
	s_add_i32 s98, s18, s82
	s_cmpk_gt_i32 s98, 0x7fff
	s_cselect_b32 s98, 0, s10
	s_cselect_b32 s99, 0, s11
	v_lshl_add_u64 v[56:57], v[4:5], 0, s[98:99]
	global_load_dwordx4 v[40:43], v[56:57], off
	global_load_dwordx4 v[44:47], v[56:57], off offset:16
	global_load_dwordx4 v[48:51], v[56:57], off offset:2048
	global_load_dwordx4 v[52:55], v[56:57], off offset:2064
	v_lshl_add_u64 v[24:25], s[84:85], 0, v[0:1]
	v_lshl_add_u64 v[26:27], s[84:85], 0, v[2:3]
	v_add_co_u32_e32 v32, vcc, s14, v24
	v_add_co_u32_e64 v34, s[2:3], s17, v26
	s_nop 0
	v_addc_co_u32_e32 v33, vcc, 0, v25, vcc
	v_addc_co_u32_e64 v35, s[2:3], 0, v27, s[2:3]
	v_max3_f32 v7, |v8|, 0, |v9|
	v_max3_f32 v7, v7, |v10|, |v11|
	v_max3_f32 v7, v7, |v12|, |v13|
	v_max3_f32 v7, v7, |v14|, |v15|
	v_max3_f32 v7, v7, |v16|, |v17|
	v_max3_f32 v7, v7, |v18|, |v19|
	v_max3_f32 v7, v7, |v20|, |v21|
	v_max3_f32 v7, v7, |v22|, |v23|
	v_cvt_pk_bf16_f32 v24, v8, v9
	v_cvt_pk_bf16_f32 v25, v10, v11
	v_mov_b32_dpp v29, v7 quad_perm:[1,0,3,2] row_mask:0xf bank_mask:0xf bound_ctrl:1
	v_max_f32_e32 v29, v29, v29
	v_max_f32_e32 v7, v7, v29
	v_cvt_pk_bf16_f32 v26, v12, v13
	v_cvt_pk_bf16_f32 v27, v14, v15
	v_mov_b32_dpp v29, v7 quad_perm:[2,3,0,1] row_mask:0xf bank_mask:0xf bound_ctrl:1
	v_max_f32_e32 v29, v29, v29
	v_max_f32_e32 v7, v7, v29
	global_store_dwordx4 v[32:33], v[24:27], off
	v_cvt_pk_bf16_f32 v28, v16, v17
	v_mov_b32_dpp v29, v7 row_half_mirror row_mask:0xf bank_mask:0xf bound_ctrl:1
	v_max_f32_e32 v29, v29, v29
	v_max_f32_e32 v7, v7, v29
	v_cvt_pk_bf16_f32 v30, v20, v21
	v_cvt_pk_bf16_f32 v31, v22, v23
	v_mov_b32_dpp v29, v7 row_mirror row_mask:0xf bank_mask:0xf bound_ctrl:1
	v_max_f32_e32 v29, v29, v29
	v_max_f32_e32 v7, v7, v29
	ds_swizzle_b32 v36, v7 offset:swizzle(SWAP,16)
	v_cvt_pk_bf16_f32 v29, v18, v19
	global_store_dwordx4 v[32:33], v[28:31], off offset:1024
	s_waitcnt lgkmcnt(0)
	v_max_f32_e32 v24, v36, v36
	v_max_f32_e32 v7, v7, v24
	v_mov_b32_e32 v24, v7
	s_nop 1
	v_permlane32_swap_b32_e32 v7, v24
	v_max_f32_e32 v24, v24, v24
	v_max_f32_e32 v7, v7, v7
	v_max_f32_e32 v7, v7, v24
	v_mul_f32_e32 v24, 0x3c010204, v7
	v_cmp_lt_f32_e32 vcc, 0, v7
	s_nop 1
	v_cndmask_b32_e32 v7, 1.0, v24, vcc
	v_div_scale_f32 v24, s[2:3], v7, v7, 1.0
	v_rcp_f32_e32 v25, v24
	v_div_scale_f32 v26, vcc, 1.0, v7, 1.0
	v_fma_f32 v27, -v24, v25, 1.0
	v_fmac_f32_e32 v25, v27, v25
	v_mul_f32_e32 v27, v26, v25
	v_fma_f32 v28, -v24, v27, v26
	v_fmac_f32_e32 v27, v28, v25
	v_fma_f32 v24, -v24, v27, v26
	v_div_fmas_f32 v24, v24, v25, v27
	v_div_fixup_f32 v24, v24, v7, 1.0
	v_fmaak_f32 v8, v8, v24, 0x4b400000
	v_fmaak_f32 v9, v9, v24, 0x4b400000
	v_fmaak_f32 v10, v10, v24, 0x4b400000
	v_fmaak_f32 v11, v11, v24, 0x4b400000
	v_fmaak_f32 v12, v12, v24, 0x4b400000
	v_fmaak_f32 v13, v13, v24, 0x4b400000
	v_fmaak_f32 v14, v14, v24, 0x4b400000
	v_fmaak_f32 v15, v15, v24, 0x4b400000
	v_fmaak_f32 v16, v16, v24, 0x4b400000
	v_fmaak_f32 v17, v17, v24, 0x4b400000
	v_fmaak_f32 v18, v18, v24, 0x4b400000
	v_fmaak_f32 v19, v19, v24, 0x4b400000
	v_fmaak_f32 v20, v20, v24, 0x4b400000
	v_fmaak_f32 v21, v21, v24, 0x4b400000
	v_fmaak_f32 v22, v22, v24, 0x4b400000
	v_fmaak_f32 v23, v23, v24, 0x4b400000
	v_perm_b32 v10, v11, v10, s15
	v_perm_b32 v8, v9, v8, s15
	v_perm_b32 v9, v15, v14, s15
	v_perm_b32 v11, v13, v12, s15
	v_perm_b32 v12, v19, v18, s15
	v_perm_b32 v13, v17, v16, s15
	v_perm_b32 v14, v23, v22, s15
	v_perm_b32 v15, v21, v20, s15
	v_perm_b32 v8, v10, v8, s16
	v_perm_b32 v9, v9, v11, s16
	v_perm_b32 v10, v12, v13, s16
	v_perm_b32 v11, v14, v15, s16
	global_store_dwordx2 v[34:35], v[8:9], off
	global_store_dwordx2 v[34:35], v[10:11], off offset:512
	s_and_saveexec_b64 s[2:3], s[0:1]
	s_cbranch_execz .LBB0_31
	s_add_u32 s20, s84, s12
	s_addc_u32 s21, s85, s13
	global_store_dword v6, v7, s[20:21]
	s_branch .LBB0_31
